# v25
# speedup vs baseline: 1.0123x; 1.0123x over previous
.LBB0_5:
	v_mad_legacy_u16 v2, v6, s8, v4
	v_lshlrev_b16_e32 v8, 15, v2
	v_lshrrev_b16_e32 v2, 1, v2
	v_cmp_lt_u32_e32 vcc, s24, v6
	v_or_b32_e32 v2, v2, v8
	s_or_b64 s[0:1], vcc, s[0:1]
	v_cmp_gt_u16_e32 vcc, s9, v2
	v_add_u32_e32 v7, 0x200, v6
	v_mov_b32_e32 v6, v7
	v_cndmask_b32_e32 v2, 0, v5, vcc
	ds_write_b64 v1, v[2:3]
	v_add_u32_e32 v1, 0x1000, v1
	s_andn2_b64 exec, exec, s[0:1]
	s_cbranch_execnz .LBB0_5
	s_or_b64 exec, exec, s[0:1]
	s_mov_b32 s34, 0
	v_cmp_eq_u32_e64 s[0:1], 0, v0
	s_and_saveexec_b64 s[8:9], s[0:1]
	v_mov_b32_e32 v1, 8
	v_mov_b32_e32 v2, 0x23420
	ds_write_b32 v2, v1
	s_or_b64 exec, exec, s[8:9]
	v_lshlrev_b32_e32 v1, 2, v131
	v_or_b32_e32 v2, 0x22200, v1
	v_or_b32_e32 v3, 0x22300, v1
	s_waitcnt lgkmcnt(0)
	s_barrier
	ds_read_b32 v2, v2
	ds_read_b32 v3, v3
	v_and_b32_e32 v202, 15, v0
	s_lshl_b32 s30, s31, 4
	v_or_b32_e32 v132, s30, v202
	s_waitcnt lgkmcnt(0)
	v_add_f32_e32 v2, v2, v3
	v_mbcnt_lo_u32_b32 v3, -1, 0
	v_mbcnt_hi_u32_b32 v3, -1, v3
	v_and_b32_e32 v4, 64, v3
	v_add_u32_e32 v4, 64, v4
	v_xor_b32_e32 v5, 32, v3
	v_cmp_lt_i32_e32 vcc, v5, v4
	v_mov_b32_e32 v133, 0
	v_lshrrev_b32_e32 v209, 4, v131
	v_cndmask_b32_e32 v5, v3, v5, vcc
	v_lshlrev_b32_e32 v200, 2, v5
	v_and_b32_e32 v203, 48, v0
	v_xor_b32_e32 v5, 16, v3
	v_cmp_lt_i32_e32 vcc, v5, v4
	v_cndmask_b32_e32 v5, v3, v5, vcc
	v_lshlrev_b32_e32 v201, 2, v5
	v_xor_b32_e32 v5, 8, v3
	v_cmp_lt_i32_e32 vcc, v5, v4
	v_cndmask_b32_e32 v5, v3, v5, vcc
	v_lshlrev_b32_e32 v205, 2, v5
	v_cmp_eq_u32_e64 s[8:9], 0, v131
	v_mov_b32_e32 v218, 0xff800000
	v_mov_b32_e32 v213, 0x23420
	v_xor_b32_e32 v5, 4, v3
	v_cmp_lt_i32_e32 vcc, v5, v4
	v_cndmask_b32_e32 v5, v3, v5, vcc
	v_lshlrev_b32_e32 v206, 2, v5
	v_xor_b32_e32 v5, 2, v3
	v_cmp_lt_i32_e32 vcc, v5, v4
	v_mov_b32_e32 v219, 0
	s_mov_b32 s35, s31
	v_cndmask_b32_e32 v5, v3, v5, vcc
	v_lshlrev_b32_e32 v207, 2, v5
	v_mov_b32_e32 v138, 0
	v_mov_b32_e32 v139, v133
	v_mov_b32_e32 v136, 0
	v_mov_b32_e32 v137, v133
	v_xor_b32_e32 v5, 1, v3
	v_cmp_lt_i32_e32 vcc, v5, v4
	v_lshlrev_b32_e32 v4, 3, v131
	v_cndmask_b32_e32 v3, v3, v5, vcc
	v_lshlrev_b32_e32 v208, 2, v3
	v_mov_b32_e32 v150, 0
	s_nop 1
	v_add_f32_dpp v2, v2, v2 row_shr:1 row_mask:0xf bank_mask:0xf
	s_nop 1
	v_add_f32_dpp v2, v2, v2 row_shr:2 row_mask:0xf bank_mask:0xf
	s_nop 1
	v_add_f32_dpp v2, v2, v2 row_shr:4 row_mask:0xf bank_mask:0xf
	s_nop 1
	v_add_f32_dpp v2, v2, v2 row_shr:8 row_mask:0xf bank_mask:0xf
	s_nop 1
	v_add_f32_dpp v2, v2, v2 row_bcast:15 row_mask:0xa bank_mask:0xf
	s_nop 1
	v_add_f32_dpp v2, v2, v2 row_bcast:31 row_mask:0xc bank_mask:0xf
	s_nop 1
	v_readlane_b32 s44, v2, 63
	s_nop 1
	v_mov_b32_e32 v2, s44
	v_add_f32_e32 v2, s43, v2
	s_mul_i32 s4, s31, 0x2200
	s_add_i32 s24, s4, 0x11000
	v_mul_f32_e32 v210, 0x3fb8aa3b, v2
	s_movk_i32 s4, 0x220
	v_mov_b32_e32 v2, s24
	v_mad_u32_u24 v5, v202, s4, v2
	v_lshlrev_b64 v[2:3], 9, v[132:133]
	v_lshl_add_u64 v[2:3], s[6:7], 0, v[2:3]
	v_lshlrev_b32_e32 v132, 5, v209
	v_add_u32_e32 v212, s24, v4
	v_mad_u32_u24 v211, v202, s4, v203
	v_lshl_add_u64 v[134:135], v[2:3], 0, v[132:133]
	v_cmp_eq_u32_e64 s[6:7], 15, v202
	v_cmp_eq_u32_e64 s[4:5], 15, v131
	v_add_u32_e32 v214, v5, v203
	v_add_u32_e32 v215, 0x800, v212
	v_add_u32_e32 v216, 0x1000, v212
	v_add_u32_e32 v217, 0x1800, v212
	v_mov_b32_e32 v151, v133
	v_mov_b32_e32 v140, 0
	v_mov_b32_e32 v141, v133
	v_mov_b32_e32 v178, 0
	v_mov_b32_e32 v179, v133
	v_mov_b32_e32 v168, 0
	v_mov_b32_e32 v169, v133
	v_mov_b32_e32 v182, 0
	v_mov_b32_e32 v183, v133
	v_mov_b32_e32 v180, 0
	v_mov_b32_e32 v181, v133
	v_mov_b32_e32 v186, 0
	v_mov_b32_e32 v187, v133
	v_mov_b32_e32 v184, 0
	v_mov_b32_e32 v185, v133
	v_mov_b32_e32 v190, 0
	v_mov_b32_e32 v191, v133
	v_mov_b32_e32 v188, 0
	v_mov_b32_e32 v189, v133
	v_mov_b32_e32 v194, 0
	v_mov_b32_e32 v195, v133
	v_mov_b32_e32 v192, 0
	v_mov_b32_e32 v193, v133
	v_mov_b32_e32 v198, 0
	v_mov_b32_e32 v199, v133
	v_mov_b32_e32 v196, 0
	v_mov_b32_e32 v197, v133
	s_cmp_eq_u32 s2, 0
	s_cselect_b64 s[24:25], -1, 0
	s_and_b64 s[24:25], s[24:25], s[10:11]
	s_and_saveexec_b64 s[26:27], s[24:25]
	s_cbranch_execz .Lp1_noinit
	global_store_dword v[254:255], v253, off
